# speedup vs baseline: 1.0236x; 1.0046x over previous
.LBB1_235:
	v_subrev_u32_e32 v0, 0x100, v0
	s_movk_i32 s0, 0xf0
	v_cmp_gt_u32_e32 vcc, s0, v0
	s_and_saveexec_b64 s[0:1], vcc
	s_cbranch_execz .Lepi_idle
	s_movk_i32 s0, 0x77
	v_mov_b32_e32 v1, 0xffffff88
	v_cmp_lt_u32_e32 vcc, s0, v0
	v_mov_b32_e32 v2, 0x44704000
	s_mov_b32 s0, 0xf800000
	v_cndmask_b32_e32 v1, 0, v1, vcc
	v_add_u32_e32 v0, v1, v0
	v_cvt_f32_u32_e32 v1, v0
	s_mov_b32 s5, 0x17800
	s_mov_b32 s4, 0x3eb17218
	v_fmac_f32_e32 v2, 0xc1000000, v1
	v_mul_f32_e32 v1, 0x4f800000, v2
	v_cmp_gt_f32_e64 s[0:1], s0, v2
	s_nop 1
	v_cndmask_b32_e64 v1, v2, v1, s[0:1]
	v_sqrt_f32_e32 v2, v1
	s_nop 0
	v_add_u32_e32 v3, -1, v2
	v_fma_f32 v4, -v3, v2, v1
	v_cmp_ge_f32_e64 s[2:3], 0, v4
	v_add_u32_e32 v4, 1, v2
	s_nop 0
	v_cndmask_b32_e64 v3, v2, v3, s[2:3]
	v_fma_f32 v2, -v4, v2, v1
	v_cmp_lt_f32_e64 s[2:3], 0, v2
	s_nop 1
	v_cndmask_b32_e64 v2, v3, v4, s[2:3]
	v_mul_f32_e32 v3, 0x37800000, v2
	v_cndmask_b32_e64 v2, v2, v3, s[0:1]
	v_mov_b32_e32 v3, 0x260
	v_cmp_class_f32_e64 s[0:1], v1, v3
	s_nop 1
	v_cndmask_b32_e64 v1, v2, v1, s[0:1]
	v_sub_f32_e32 v1, 0x41f80000, v1
	v_mul_f32_e32 v1, 0.5, v1
	v_cvt_i32_f32_e32 v1, v1
	s_and_b64 s[0:1], exec, s[16:17]
	s_cselect_b32 s2, s40, s38
	s_cselect_b32 s3, s39, s33
	v_sub_u32_e32 v2, 31, v1
	v_mul_lo_u32 v2, v2, v1
	v_lshrrev_b32_e32 v3, 31, v2
	v_add_u32_e32 v2, v2, v3
	v_ashrrev_i32_e32 v2, 1, v2
	v_cmp_gt_i32_e64 s[0:1], v2, v0
	s_nop 1
	v_subbrev_co_u32_e64 v1, s[0:1], 0, v1, s[0:1]
	v_add_u32_e32 v2, 1, v1
	v_sub_u32_e32 v3, 30, v1
	v_mul_lo_u32 v3, v2, v3
	v_lshrrev_b32_e32 v4, 31, v3
	v_add_u32_e32 v3, v3, v4
	v_ashrrev_i32_e32 v3, 1, v3
	v_cmp_gt_i32_e64 s[0:1], v3, v0
	s_nop 1
	v_cndmask_b32_e64 v12, v2, v1, s[0:1]
	v_sub_u32_e32 v1, 31, v12
	v_mul_lo_u32 v1, v1, v12
	v_lshrrev_b32_e32 v2, 31, v1
	v_add_u32_e32 v1, v1, v2
	v_ashrrev_i32_e32 v1, 1, v1
	v_sub_u32_e32 v0, v0, v1
	v_cndmask_b32_e64 v1, 0, 16, vcc
	v_lshl_or_b32 v1, s2, 5, v1
	v_add_u32_e32 v1, v1, v12
	v_sub_u32_e32 v2, 0xff, v1
	v_mul_lo_u32 v1, v2, v1
	v_lshrrev_b32_e32 v2, 31, v1
	v_add_u32_e32 v1, v1, v2
	v_ashrrev_i32_e32 v1, 1, v1
	v_add3_u32 v13, v12, v0, 1
	v_add_u32_e32 v0, v1, v0
	v_ashrrev_i32_e32 v1, 31, v0
	v_mov_b32_e32 v2, 0x1fc0
	v_mad_u64_u32 v[0:1], s[0:1], s3, v2, v[0:1]
	v_mad_u64_u32 v[4:5], s[0:1], v0, 24, s[10:11]
	v_mov_b32_e32 v0, 0x17800
	v_lshl_add_u32 v14, v12, 2, v0
	v_mov_b32_e32 v0, 0x60
	v_cndmask_b32_e32 v15, 0, v0, vcc
	v_or_b32_e32 v2, 16, v15
	v_add_lshl_u32 v3, v2, v12, 6
	v_add_u32_e32 v2, v2, v13
	v_lshl_add_u32 v6, v2, 6, v14
	v_add_u32_e32 v2, 32, v15
	v_add_lshl_u32 v7, v2, v12, 6
	v_add_u32_e32 v2, v2, v13
	v_lshl_add_u32 v8, v2, 6, v14
	v_add_u32_e32 v2, 48, v15
	v_mad_i32_i24 v5, v1, 24, v5
	v_add_lshl_u32 v0, v15, v12, 6
	v_lshlrev_b32_e32 v16, 2, v13
	v_add_u32_e32 v1, v15, v13
	v_add_lshl_u32 v9, v2, v12, 6
	v_add_u32_e32 v17, 64, v15
	v_add_u32_e32 v15, 0x50, v15
	v_add3_u32 v0, v0, v16, s5
	v_lshl_add_u32 v1, v1, 6, v14
	v_add3_u32 v3, v3, v16, s5
	v_add3_u32 v7, v7, v16, s5
	v_add3_u32 v9, v9, v16, s5
	v_add_u32_e32 v2, v2, v13
	v_add_lshl_u32 v18, v17, v12, 6
	v_add_lshl_u32 v12, v15, v12, 6
	s_load_dwordx4 s[0:3], s[14:15], 0x0
	v_lshl_add_u32 v10, v2, 6, v14
	s_waitcnt lgkmcnt(0)
	s_barrier
	ds_read_b32 v0, v0
	ds_read_b32 v2, v1
	ds_read_b32 v1, v3
	ds_read_b32 v3, v6
	ds_read_b32 v6, v7
	ds_read_b32 v8, v8
	ds_read_b32 v7, v9
	ds_read_b32 v9, v10
	v_add3_u32 v18, v18, v16, s5
	v_add3_u32 v16, v12, v16, s5
	v_add_u32_e32 v12, v15, v13
	v_add_u32_e32 v17, v17, v13
	v_lshl_add_u32 v15, v12, 6, v14
	s_load_dwordx2 s[6:7], s[14:15], 0x10
	v_lshl_add_u32 v17, v17, 6, v14
	ds_read_b32 v12, v18
	ds_read_b32 v14, v17
	ds_read_b32 v13, v16
	ds_read_b32 v15, v15
	s_waitcnt lgkmcnt(0)
	v_pk_add_f32 v[0:1], v[0:1], v[2:3]
	v_mov_b32_e32 v2, s2
	v_mov_b32_e32 v3, s3
	v_mov_b64_e32 v[10:11], s[0:1]
	v_pk_add_f32 v[6:7], v[6:7], v[8:9]
	v_pk_fma_f32 v[0:1], v[0:1], s[4:5], v[10:11] op_sel_hi:[1,0,1]
	v_pk_fma_f32 v[2:3], v[6:7], s[4:5], v[2:3] op_sel_hi:[1,0,1]
	global_store_dwordx4 v[4:5], v[0:3], off
	s_nop 1
	v_pk_add_f32 v[0:1], v[12:13], v[14:15]
	v_mov_b64_e32 v[2:3], s[6:7]
	v_pk_fma_f32 v[0:1], v[0:1], s[4:5], v[2:3] op_sel_hi:[1,0,1]
	global_store_dwordx2 v[4:5], v[0:1], off offset:16
	s_endpgm
.Lepi_idle:
	s_waitcnt lgkmcnt(0)
	s_barrier
	s_endpgm
